# baseline (speedup 1.0000x reference)
_Z7k2_elimPKjPKiPiS2_PfP15HIP_vector_typeIiLj4EEPKfS4_PtSA_:
	s_load_dwordx2 s[6:7], s[0:1], 0x8
	s_mov_b64 s[4:5], -1
	s_cmpk_lt_u32 s2, 0x80
	v_lshrrev_b32_e32 v1, 6, v0
	v_lshlrev_b32_e32 v14, 2, v0
	s_cbranch_scc0 .LBB1_28
	s_load_dwordx2 s[4:5], s[0:1], 0x0
	s_load_dwordx2 s[8:9], s[0:1], 0x18
	s_lshr_b32 s14, s2, 6
	s_mov_b32 s15, 0
	s_and_b32 s3, s2, 63
	s_lshl_b64 s[10:11], s[14:15], 11
	s_waitcnt lgkmcnt(0)
	s_add_u32 s8, s8, s10
	s_addc_u32 s9, s9, s11
	s_lshl_b32 s10, s3, 5
	s_add_u32 s8, s8, s10
	s_addc_u32 s9, s9, 0
	s_lshl_b64 s[10:11], s[14:15], 15
	s_add_u32 s4, s4, s10
	s_addc_u32 s5, s5, s11
	v_lshlrev_b32_e32 v2, 4, v0
	v_mov_b32_e32 v3, 0
	v_lshl_add_u64 v[4:5], s[4:5], 0, v[2:3]
	s_movk_i32 s10, 0x2000
	v_readfirstlane_b32 s46, v1
	s_cmp_lt_u32 s46, 4
	s_cbranch_scc1 .Lk2_noprio
	s_setprio 1
.Lk2_noprio:
	s_mov_b64 s[44:45], 0x2000
	s_lshl_b32 s46, s46, 10
	s_mov_b32 m0, s46
	v_lshl_add_u64 v[20:21], v[4:5], 0, s[44:45]
	global_load_lds_dwordx4 v[4:5], off
	s_add_u32 s47, s46, 0x2000
	s_mov_b32 m0, s47
	v_lshl_add_u64 v[22:23], v[20:21], 0, s[44:45]
	global_load_lds_dwordx4 v[20:21], off
	s_add_u32 s47, s46, 0x4000
	s_mov_b32 m0, s47
	v_lshl_add_u64 v[20:21], v[22:23], 0, s[44:45]
	global_load_lds_dwordx4 v[22:23], off
	s_add_u32 s47, s46, 0x6000
	s_mov_b32 m0, s47
	s_movk_i32 s4, 0x1000
	global_load_lds_dwordx4 v[20:21], off
	v_lshl_or_b32 v4, s14, 12, v0
	v_mov_b32_e32 v5, v3
	v_lshl_add_u64 v[4:5], v[4:5], 2, s[6:7]
	v_add_co_u32_e32 v24, vcc, s4, v4
	s_cmp_lg_u32 s3, 0
	s_nop 0
	v_addc_co_u32_e32 v25, vcc, 0, v5, vcc
	v_add_co_u32_e32 v26, vcc, s10, v4
	s_nop 1
	v_addc_co_u32_e32 v27, vcc, 0, v5, vcc
	global_load_dword v15, v[26:27], off offset:-4096
	global_load_dword v28, v[26:27], off
	global_load_dword v29, v[26:27], off offset:2048
	v_add_co_u32_e32 v26, vcc, 0x3000, v4
	s_nop 1
	v_addc_co_u32_e32 v27, vcc, 0, v5, vcc
	global_load_dword v30, v[4:5], off
	global_load_dword v31, v[4:5], off offset:2048
	global_load_dword v32, v[24:25], off offset:2048
	global_load_dword v33, v[26:27], off
	global_load_dword v34, v[26:27], off offset:2048
	v_lshlrev_b32_e32 v4, 2, v1
	global_load_dword v5, v4, s[8:9]
	s_waitcnt vmcnt(4)
	v_max3_i32 v4, v30, v31, v15
	s_waitcnt vmcnt(3)
	v_max3_i32 v4, v4, v32, v28
	s_waitcnt vmcnt(2)
	v_max3_i32 v4, v4, v29, v33
	s_waitcnt vmcnt(1)
	v_max3_i32 v4, v4, v34, -1
	ds_write_b32 v14, v4 offset:32768
	s_cbranch_scc0 .LBB1_34
	v_or_b32_e32 v3, 0x8000, v14
	v_cmp_gt_u32_e32 vcc, 16, v0
	s_and_saveexec_b64 s[4:5], vcc
